# L0 dilated sparse attention: ALiBi bias + window mask from a per-wave LDS table (ds_read2 + pk_add) instead of per-slot VALU; L1 dense epilogue dword stores
# speedup vs baseline: 1.0077x; 1.0009x over previous
; #define LAS __attribute__((address_space(3)))
; __global__ void __launch_bounds__(NTHR, 2) fwd(Params p) {
;     extern __shared__ __attribute__((aligned(16))) unsigned char lds_raw[];
;     LAS unsigned char* lds = (LAS unsigned char*)lds_raw;
;     const int tid0 = threadIdx.x, bid = blockIdx.x, G = gridDim.x;
;     const int wv = __builtin_amdgcn_readfirstlane(tid0 >> 6);
;     const int vcu = (G % 8 == 0) ? (bid % 8) * (G / 8) + bid / 8 : bid;
;     unsigned* ctl = (unsigned*)(p.ws + WS_CTL);
;     if (tid0 < 4) ((LAS unsigned*)(lds + MISC_OFF))[tid0] = 0u;
;     __syncthreads();
;     XcdBarrier bar; bar.bar = ctl + CW_BAR; bar.x = 0; bar.st = (volatile LAS unsigned*)(lds + MISC_OFF);
;     if (N_LAUNCH_MODE == 1) bar = xcd_barrier_post(ctl + CW_BAR, (volatile LAS unsigned*)(lds + MISC_OFF));
_Z3fwd6Params:
	s_mov_b64 s[76:77], s[0:1]
	s_mov_b32 s101, 0
	s_load_dword s50, s[0:1], 0xf8
	s_nop 0
	s_load_dwordx2 s[0:1], s[0:1], 0xe8
	s_mov_b32 s30, s2
	s_add_u32 s2, s76, 0xf8
	s_addc_u32 s3, s77, 0
	v_readfirstlane_b32 s8, v0
	v_writelane_b32 v252, s2, 0
	s_nop 1
	v_writelane_b32 v252, s3, 1
	s_waitcnt lgkmcnt(0)
	s_and_b32 s2, s50, 7
	s_cmp_lg_u32 s2, 0
	s_mov_b32 s2, s30
	v_writelane_b32 v252, s2, 2
	s_cbranch_scc1 .LBB0_1
	s_getpc_b64 s[98:99]

; template <class P>
; __device__ __forceinline__ void sparse8_wave(P& pol, LAS unsigned char* wll, int lane) {
;     ...
;         float pmax = -INFINITY;
; #pragma unroll
;         for (int r = 0; r < 16; ++r) { p0[r] = pol.adj(ti, r, p0[r]); p1[r] = pol.adj(ti, 16 + r, p1[r]); pmax = fmaxf(pmax, fmaxf(p0[r], p1[r])); }
;         { auto rr = __builtin_amdgcn_permlane32_swap(__float_as_uint(pmax), __float_as_uint(pmax), false, false);
;           pmax = fmaxf(__uint_as_float(rr[0]), __uint_as_float(rr[1])); }
;     __device__ __forceinline__ float adj(const TI& ti, int slot, float s) const {
;         const float fd = ti.fb + (float)slot;
;         return __builtin_fabsf(fd) <= 64.f ? fmaf(__builtin_fabsf(fd), ti.ncd, s) : -INFINITY;
;     }
.LBB0_567:
	v_readfirstlane_b32 s6, v162
	s_cmp_eq_u32 s6, s101
	s_cbranch_scc1 .Lsp0_tab_ok
	s_mov_b32 s101, s6
	s_add_i32 s7, s61, 0x4100
	v_mbcnt_lo_u32_b32 v112, -1, 0
	v_mbcnt_hi_u32_b32 v112, -1, v112
	v_lshl_add_u32 v113, v112, 2, s7
	v_add_u32_e32 v114, 0xffffffa0, v112
	v_cvt_f32_i32_e32 v114, v114
	v_mul_f32_e64 v115, |v114|, v162
	v_cmp_le_f32_e64 vcc, |v114|, s16
	s_nop 1
	v_cndmask_b32_e32 v115, v250, v115, vcc
	ds_write_b32 v113, v115
	v_add_u32_e32 v114, 0xffffffe0, v112
	v_cvt_f32_i32_e32 v114, v114
	v_mul_f32_e64 v115, |v114|, v162
	v_cmp_le_f32_e64 vcc, |v114|, s16
	s_nop 1
	v_cndmask_b32_e32 v115, v250, v115, vcc
	ds_write_b32 v113, v115 offset:256
	v_add_u32_e32 v114, 32, v112
	v_cvt_f32_i32_e32 v114, v114
	v_mul_f32_e64 v115, |v114|, v162
	v_cmp_le_f32_e64 vcc, |v114|, s16
	s_nop 1
	v_cndmask_b32_e32 v115, v250, v115, vcc
	ds_write_b32 v113, v115 offset:512
	v_add_u32_e32 v114, 0x60, v112
	v_cvt_f32_i32_e32 v114, v114
	v_mul_f32_e64 v115, |v114|, v162
	v_cmp_le_f32_e64 vcc, |v114|, s16
	s_nop 1
	v_cndmask_b32_e32 v115, v250, v115, vcc
	ds_write_b32 v113, v115 offset:768
.Lsp0_tab_ok:
	s_waitcnt lgkmcnt(0)
	v_mfma_f32_32x32x64_f8f6f4 v[112:127], v[96:103], v[128:135], v[80:95]
	v_mfma_f32_32x32x64_f8f6f4 v[112:127], v[104:111], v[136:143], v[112:127]
	v_mfma_f32_32x32x64_f8f6f4 v[96:111], v[144:151], v[128:135], v[80:95]
	v_mfma_f32_32x32x64_f8f6f4 v[96:111], v[152:159], v[136:143], v[96:111]
	v_cvt_i32_f32_e32 v162, v164
	v_max_i32_e32 v162, 0xffffffa0, v162
	v_min_i32_e32 v162, 0x41, v162
	s_add_i32 s6, s61, 0x4280
	v_lshl_add_u32 v162, v162, 2, s6
	ds_read2_b32 v[144:145], v162 offset0:1 offset1:0
	ds_read2_b32 v[148:149], v162 offset0:3 offset1:2
	ds_read2_b32 v[152:153], v162 offset0:5 offset1:4
	ds_read2_b32 v[156:157], v162 offset0:7 offset1:6
	ds_read2_b32 v[184:185], v162 offset0:9 offset1:8
	ds_read2_b32 v[188:189], v162 offset0:11 offset1:10
	ds_read2_b32 v[192:193], v162 offset0:13 offset1:12
	ds_read_b32 v196, v162 offset:56
	ds_read_b32 v164, v162 offset:60
	ds_read2_b32 v[146:147], v162 offset0:17 offset1:16
	ds_read2_b32 v[150:151], v162 offset0:19 offset1:18
	ds_read2_b32 v[154:155], v162 offset0:21 offset1:20
	ds_read2_b32 v[158:159], v162 offset0:23 offset1:22
	ds_read2_b32 v[186:187], v162 offset0:25 offset1:24
	ds_read2_b32 v[190:191], v162 offset0:27 offset1:26
	ds_read2_b32 v[194:195], v162 offset0:29 offset1:28
	ds_read_b32 v197, v162 offset:120
	ds_read_b32 v162, v162 offset:124
	s_waitcnt lgkmcnt(0)
	v_pk_add_f32 v[144:145], v[144:145], v[112:113] op_sel:[0,1] op_sel_hi:[1,0]
	v_pk_add_f32 v[148:149], v[148:149], v[114:115] op_sel:[0,1] op_sel_hi:[1,0]
	v_pk_add_f32 v[152:153], v[152:153], v[116:117] op_sel:[0,1] op_sel_hi:[1,0]
	v_pk_add_f32 v[156:157], v[156:157], v[118:119] op_sel:[0,1] op_sel_hi:[1,0]
	v_pk_add_f32 v[184:185], v[184:185], v[120:121] op_sel:[0,1] op_sel_hi:[1,0]
	v_pk_add_f32 v[188:189], v[188:189], v[122:123] op_sel:[0,1] op_sel_hi:[1,0]
	v_pk_add_f32 v[192:193], v[192:193], v[124:125] op_sel:[0,1] op_sel_hi:[1,0]
	v_add_f32_e32 v196, v196, v126
	v_add_f32_e32 v164, v164, v127
	v_pk_add_f32 v[146:147], v[146:147], v[96:97] op_sel:[0,1] op_sel_hi:[1,0]
	v_pk_add_f32 v[150:151], v[150:151], v[98:99] op_sel:[0,1] op_sel_hi:[1,0]
	v_pk_add_f32 v[154:155], v[154:155], v[100:101] op_sel:[0,1] op_sel_hi:[1,0]
	v_pk_add_f32 v[158:159], v[158:159], v[102:103] op_sel:[0,1] op_sel_hi:[1,0]
	v_pk_add_f32 v[186:187], v[186:187], v[104:105] op_sel:[0,1] op_sel_hi:[1,0]
	v_pk_add_f32 v[190:191], v[190:191], v[106:107] op_sel:[0,1] op_sel_hi:[1,0]
	v_pk_add_f32 v[194:195], v[194:195], v[108:109] op_sel:[0,1] op_sel_hi:[1,0]
	v_add_f32_e32 v197, v197, v110
	v_add_f32_e32 v162, v162, v111
	v_max3_f32 v96, v145, v144, v149
	v_max3_f32 v97, v148, v153, v152
	v_max3_f32 v96, v96, v157, v156
	v_max3_f32 v97, v97, v185, v184
	v_max3_f32 v96, v96, v189, v188
	v_max3_f32 v97, v97, v193, v192
	v_max3_f32 v96, v96, v196, v164
	v_max3_f32 v97, v97, v147, v146
	v_max3_f32 v96, v96, v151, v150
	v_max3_f32 v97, v97, v155, v154
	v_max3_f32 v96, v96, v159, v158
	v_max3_f32 v97, v97, v187, v186
	v_max3_f32 v96, v96, v191, v190
	v_max3_f32 v97, v97, v195, v194
	v_max3_f32 v96, v96, v197, v162
	v_max_f32_e32 v96, v96, v97
	s_xor_b64 s[6:7], s[0:1], -1
	v_mov_b32_e32 v97, v96
	s_nop 1
	v_permlane32_swap_b32_e32 v96, v97
	v_max_f32_e32 v97, v97, v97
	v_max_f32_e32 v96, v96, v96
	v_max_f32_e32 v96, v96, v97
	v_cmp_lg_f32_e64 s[42:43], s11, v96
	s_and_b64 s[6:7], s[42:43], s[6:7]
	v_cmp_lt_f32_e32 vcc, s10, v96
	s_or_b64 vcc, vcc, s[6:7]
	s_nop 0
	v_cndmask_b32_e32 v96, 0, v96, vcc
	v_cmp_neq_f32_e32 vcc, 0, v96
	s_cbranch_vccz .LBB0_571
	s_and_saveexec_b64 s[8:9], s[38:39]
	s_cbranch_execz .LBB0_570
	v_exp_f32_e64 v80, -v96
	s_nop 0
	v_cndmask_b32_e64 v80, v80, 1.0, s[6:7]
	ds_write_b32 v178, v80 offset:16512

; __global__ void __launch_bounds__(NTHR, 2) fwd(Params p) {
	.amdhsa_kernel _Z3fwd6Params
		.amdhsa_group_segment_fixed_size 0
		.amdhsa_private_segment_fixed_size 0
		.amdhsa_kernarg_size 504
		.amdhsa_user_sgpr_count 2
		.amdhsa_user_sgpr_dispatch_ptr 0
		.amdhsa_user_sgpr_queue_ptr 0
		.amdhsa_user_sgpr_kernarg_segment_ptr 1
		.amdhsa_user_sgpr_dispatch_id 0
		.amdhsa_user_sgpr_kernarg_preload_length 0
		.amdhsa_user_sgpr_kernarg_preload_offset 0
		.amdhsa_user_sgpr_private_segment_size 0
		.amdhsa_uses_dynamic_stack 0
		.amdhsa_enable_private_segment 0
		.amdhsa_system_sgpr_workgroup_id_x 1
		.amdhsa_system_sgpr_workgroup_id_y 0
		.amdhsa_system_sgpr_workgroup_id_z 0
		.amdhsa_system_sgpr_workgroup_info 0
		.amdhsa_system_vgpr_workitem_id 0
		.amdhsa_next_free_vgpr 256
		.amdhsa_next_free_sgpr 102
		.amdhsa_accum_offset 256
		.amdhsa_reserve_vcc 1
		.amdhsa_float_round_mode_32 0
		.amdhsa_float_round_mode_16_64 0
		.amdhsa_float_denorm_mode_32 3
		.amdhsa_float_denorm_mode_16_64 3
		.amdhsa_dx10_clamp 1
		.amdhsa_ieee_mode 1
		.amdhsa_fp16_overflow 0
		.amdhsa_tg_split 0
		.amdhsa_exception_fp_ieee_invalid_op 0
		.amdhsa_exception_fp_denorm_src 0
		.amdhsa_exception_fp_ieee_div_zero 0
		.amdhsa_exception_fp_ieee_overflow 0
		.amdhsa_exception_fp_ieee_underflow 0
		.amdhsa_exception_fp_ieee_inexact 0
		.amdhsa_exception_int_div_zero 0
	.end_amdhsa_kernel

; __global__ void __launch_bounds__(NTHR, 2) fwd(Params p) {
amdhsa.kernels:
  - .agpr_count:     0
    .args:
      - .offset:         0
        .size:           248
        .value_kind:     by_value
      - .offset:         248
        .size:           4
        .value_kind:     hidden_block_count_x
      - .offset:         252
        .size:           4
        .value_kind:     hidden_block_count_y
      - .offset:         256
        .size:           4
        .value_kind:     hidden_block_count_z
      - .offset:         260
        .size:           2
        .value_kind:     hidden_group_size_x
      - .offset:         262
        .size:           2
        .value_kind:     hidden_group_size_y
      - .offset:         264
        .size:           2
        .value_kind:     hidden_group_size_z
      - .offset:         266
        .size:           2
        .value_kind:     hidden_remainder_x
      - .offset:         268
        .size:           2
        .value_kind:     hidden_remainder_y
      - .offset:         270
        .size:           2
        .value_kind:     hidden_remainder_z
      - .offset:         288
        .size:           8
        .value_kind:     hidden_global_offset_x
      - .offset:         296
        .size:           8
        .value_kind:     hidden_global_offset_y
      - .offset:         304
        .size:           8
        .value_kind:     hidden_global_offset_z
      - .offset:         312
        .size:           2
        .value_kind:     hidden_grid_dims
      - .offset:         368
        .size:           4
        .value_kind:     hidden_dynamic_lds_size
    .group_segment_fixed_size: 0
    .kernarg_segment_align: 8
    .kernarg_segment_size: 504
    .language:       OpenCL C
    .language_version:
      - 2
      - 0
    .max_flat_workgroup_size: 512
    .name:           _Z3fwd6Params
    .private_segment_fixed_size: 0
    .sgpr_count:     108
    .sgpr_spill_count: 260
    .symbol:         _Z3fwd6Params.kd
    .uniform_work_group_size: 1
    .uses_dynamic_stack: false
    .vgpr_count:     256
    .vgpr_spill_count: 0
    .wavefront_size: 64
